# first accumulate group after re-init uses C=0 unconditionally (select matrix is zero outside the block): accumulator zeroing MFMAs and two compares removed from every flush
# speedup vs baseline: 1.0773x; 1.0056x over previous
.LBB1_149:
	v_sub_u32_e32 v3, v230, v194
	s_waitcnt lgkmcnt(0)
	v_add_u32_e32 v4, v3, v234
	v_add_u32_e32 v5, -1, v3
	v_med3_i32 v4, v4, -1, 32
	v_med3_i32 v5, v5, -1, 32
	v_cvt_f32_i32_e32 v4, v4
	v_cvt_f32_i32_e32 v5, v5
	v_cvt_pk_f16_f32 v14, v4, v4
	v_cvt_pk_f16_f32 v15, v5, v5
	v_pk_add_f16 v3, v14, s73 neg_lo:[0,1] neg_hi:[0,1]
	v_pk_add_f16 v4, s73, v15 neg_lo:[0,1] neg_hi:[0,1]
	v_pk_min_f16 v6, v3, v4 clamp
	v_pk_add_f16 v5, v14, s74 neg_lo:[0,1] neg_hi:[0,1]
	v_pk_add_f16 v16, s74, v15 neg_lo:[0,1] neg_hi:[0,1]
	v_pk_min_f16 v7, v5, v16 clamp
	v_pk_add_f16 v3, v14, s75 neg_lo:[0,1] neg_hi:[0,1]
	v_pk_add_f16 v4, s75, v15 neg_lo:[0,1] neg_hi:[0,1]
	v_pk_min_f16 v8, v3, v4 clamp
	v_pk_add_f16 v5, v14, s76 neg_lo:[0,1] neg_hi:[0,1]
	v_pk_add_f16 v16, s76, v15 neg_lo:[0,1] neg_hi:[0,1]
	v_pk_min_f16 v9, v5, v16 clamp
	s_nop 1
	v_mfma_f32_32x32x16_f16 v[66:81], v[198:201], v[6:9], 0
	v_mfma_f32_32x32x16_f16 v[50:65], v[206:209], v[6:9], 0
	v_mfma_f32_32x32x16_f16 v[34:49], v[214:217], v[6:9], 0
	v_mfma_f32_32x32x16_f16 v[18:33], v[222:225], v[6:9], 0
.LBB1_151:
	v_cmp_gt_i32_e32 vcc, s18, v231
	v_cmp_lt_i32_e64 s[2:3], s19, v249
	s_and_b64 s[8:9], vcc, s[2:3]
	s_and_saveexec_b64 s[2:3], s[8:9]
	s_cbranch_execz .LBB1_153
	v_pk_add_f16 v3, v14, s77 neg_lo:[0,1] neg_hi:[0,1]
	v_pk_add_f16 v4, s77, v15 neg_lo:[0,1] neg_hi:[0,1]
	v_pk_min_f16 v6, v3, v4 clamp
	v_pk_add_f16 v5, v14, s78 neg_lo:[0,1] neg_hi:[0,1]
	v_pk_add_f16 v16, s78, v15 neg_lo:[0,1] neg_hi:[0,1]
	v_pk_min_f16 v7, v5, v16 clamp
	v_pk_add_f16 v3, v14, s79 neg_lo:[0,1] neg_hi:[0,1]
	v_pk_add_f16 v4, s79, v15 neg_lo:[0,1] neg_hi:[0,1]
	v_pk_min_f16 v8, v3, v4 clamp
	v_pk_add_f16 v5, v14, s80 neg_lo:[0,1] neg_hi:[0,1]
	v_pk_add_f16 v16, s80, v15 neg_lo:[0,1] neg_hi:[0,1]
	v_pk_min_f16 v9, v5, v16 clamp
	s_nop 1
	v_mfma_f32_32x32x16_f16 v[66:81], v[202:205], v[6:9], v[66:81]
	v_mfma_f32_32x32x16_f16 v[50:65], v[210:213], v[6:9], v[50:65]
	v_mfma_f32_32x32x16_f16 v[34:49], v[218:221], v[6:9], v[34:49]
	v_mfma_f32_32x32x16_f16 v[18:33], v[226:229], v[6:9], v[18:33]

.Lpeel_join:
	v_cmp_ge_i32_e32 vcc, s18, v249
	s_mov_b64 s[8:9], 0
	s_and_saveexec_b64 s[2:3], vcc
	s_cbranch_execz .LBB1_148
	s_setprio 3
	v_cmp_gt_i32_e32 vcc, s12, v235
	s_and_b64 s[10:11], s[0:1], vcc
	ds_read_b128 v[82:85], v245 offset:32768
	ds_read_b128 v[86:89], v245 offset:32784
	ds_read_b128 v[90:93], v245 offset:32800
	ds_read_b128 v[94:97], v245 offset:32816
	ds_read_b128 v[98:101], v245 offset:32832
	ds_read_b128 v[102:105], v245 offset:32848
	ds_read_b128 v[106:109], v245 offset:32864
	ds_read_b128 v[110:113], v245 offset:32880
	ds_read_b128 v[114:117], v246 offset:0
	ds_read_b128 v[118:121], v246 offset:8192
	ds_read_b128 v[122:125], v246 offset:1024
	ds_read_b128 v[126:129], v246 offset:9216
	v_cvt_f32_i32_e32 v16, v234
	v_cvt_pk_f16_f32 v4, v66, v67
	v_cvt_pk_f16_f32 v5, v68, v69
	v_cvt_pk_f16_f32 v6, v70, v71
	v_cvt_pk_f16_f32 v7, v72, v73
	v_cvt_pk_f16_f32 v8, v74, v75
	v_cvt_pk_f16_f32 v9, v76, v77
	v_cvt_pk_f16_f32 v10, v78, v79
	v_cvt_pk_f16_f32 v11, v80, v81
	s_waitcnt lgkmcnt(8)
	v_pk_mul_f32 v[162:163], v[82:83], v[16:17] op_sel_hi:[1,0]
	v_pk_mul_f32 v[164:165], v[84:85], v[16:17] op_sel_hi:[1,0]
	v_pk_mul_f32 v[166:167], v[86:87], v[16:17] op_sel_hi:[1,0]
	v_pk_mul_f32 v[168:169], v[88:89], v[16:17] op_sel_hi:[1,0]
	v_pk_mul_f32 v[170:171], v[90:91], v[16:17] op_sel_hi:[1,0]
	v_pk_mul_f32 v[172:173], v[92:93], v[16:17] op_sel_hi:[1,0]
	v_pk_mul_f32 v[174:175], v[94:95], v[16:17] op_sel_hi:[1,0]
	v_pk_mul_f32 v[176:177], v[96:97], v[16:17] op_sel_hi:[1,0]
	ds_read_b128 v[130:133], v246 offset:2048
	ds_read_b128 v[134:137], v246 offset:10240
	ds_read_b128 v[138:141], v246 offset:3072
	ds_read_b128 v[142:145], v246 offset:11264
	s_waitcnt lgkmcnt(4)
	v_mfma_f32_32x32x16_f16 v[162:177], v[114:117], v[4:7], v[162:177]
	v_pk_mul_f32 v[146:147], v[98:99], v[16:17] op_sel_hi:[1,0]
	v_pk_mul_f32 v[148:149], v[100:101], v[16:17] op_sel_hi:[1,0]
	v_pk_mul_f32 v[150:151], v[102:103], v[16:17] op_sel_hi:[1,0]
	v_pk_mul_f32 v[152:153], v[104:105], v[16:17] op_sel_hi:[1,0]
	v_pk_mul_f32 v[154:155], v[106:107], v[16:17] op_sel_hi:[1,0]
	v_pk_mul_f32 v[156:157], v[108:109], v[16:17] op_sel_hi:[1,0]
	v_pk_mul_f32 v[158:159], v[110:111], v[16:17] op_sel_hi:[1,0]
	v_pk_mul_f32 v[160:161], v[112:113], v[16:17] op_sel_hi:[1,0]
	s_nop 1
	v_mfma_f32_32x32x16_f16 v[146:161], v[118:121], v[4:7], v[146:161]
	v_cvt_pk_f16_f32 v12, v50, v51
	v_cvt_pk_f16_f32 v13, v52, v53
	v_cvt_pk_f16_f32 v14, v54, v55
	v_cvt_pk_f16_f32 v15, v56, v57
	v_mfma_f32_32x32x16_f16 v[162:177], v[122:125], v[8:11], v[162:177]
	v_cvt_pk_f16_f32 v252, v58, v59
	v_cvt_pk_f16_f32 v253, v60, v61
	v_cvt_pk_f16_f32 v254, v62, v63
	v_cvt_pk_f16_f32 v255, v64, v65
	v_mfma_f32_32x32x16_f16 v[146:161], v[126:129], v[8:11], v[146:161]
	ds_read_b128 v[82:85], v246 offset:4096
	ds_read_b128 v[86:89], v246 offset:12288
	ds_read_b128 v[90:93], v246 offset:5120
	ds_read_b128 v[94:97], v246 offset:13312
	s_waitcnt lgkmcnt(4)
	v_mfma_f32_32x32x16_f16 v[162:177], v[130:133], v[12:15], v[162:177]
	v_cvt_pk_f16_f32 v4, v34, v35
	v_cvt_pk_f16_f32 v5, v36, v37
	v_mfma_f32_32x32x16_f16 v[146:161], v[134:137], v[12:15], v[146:161]
	v_cvt_pk_f16_f32 v6, v38, v39
	v_cvt_pk_f16_f32 v7, v40, v41
	v_mfma_f32_32x32x16_f16 v[162:177], v[138:141], v[252:255], v[162:177]
	v_cvt_pk_f16_f32 v8, v42, v43
	v_cvt_pk_f16_f32 v9, v44, v45
	v_mfma_f32_32x32x16_f16 v[146:161], v[142:145], v[252:255], v[146:161]
	v_cvt_pk_f16_f32 v10, v46, v47
	v_cvt_pk_f16_f32 v11, v48, v49
	ds_read_b128 v[98:101], v246 offset:6144
	ds_read_b128 v[102:105], v246 offset:14336
	ds_read_b128 v[106:109], v246 offset:7168
	ds_read_b128 v[110:113], v246 offset:15360
	s_waitcnt lgkmcnt(4)
	v_mfma_f32_32x32x16_f16 v[162:177], v[82:85], v[4:7], v[162:177]
	v_cvt_pk_f16_f32 v12, v18, v19
	v_cvt_pk_f16_f32 v13, v20, v21
	v_mfma_f32_32x32x16_f16 v[146:161], v[86:89], v[4:7], v[146:161]
	v_cvt_pk_f16_f32 v14, v22, v23
	v_cvt_pk_f16_f32 v15, v24, v25
	v_mfma_f32_32x32x16_f16 v[162:177], v[90:93], v[8:11], v[162:177]
	v_cvt_pk_f16_f32 v252, v26, v27
	v_cvt_pk_f16_f32 v253, v28, v29
	v_mfma_f32_32x32x16_f16 v[146:161], v[94:97], v[8:11], v[146:161]
	v_cvt_pk_f16_f32 v254, v30, v31
	v_cvt_pk_f16_f32 v255, v32, v33
	ds_read_b128 v[18:21], v246 offset:16384
	ds_read_b128 v[22:25], v246 offset:17408
	ds_read_b128 v[26:29], v246 offset:18432
	ds_read_b128 v[30:33], v246 offset:19456
	s_waitcnt lgkmcnt(4)
	v_mfma_f32_32x32x16_f16 v[162:177], v[98:101], v[12:15], v[162:177]
	v_mfma_f32_32x32x16_f16 v[146:161], v[102:105], v[12:15], v[146:161]
	v_mfma_f32_32x32x16_f16 v[162:177], v[106:109], v[252:255], v[162:177]
	v_mfma_f32_32x32x16_f16 v[146:161], v[110:113], v[252:255], v[146:161]
	ds_read_b128 v[130:133], v247 offset:33024
	ds_read_b128 v[134:137], v247 offset:33040
	ds_read_b128 v[138:141], v247 offset:33056
	ds_read_b128 v[142:145], v247 offset:33072
	ds_read_b128 v[114:117], v247 offset:33088
	ds_read_b128 v[118:121], v247 offset:33104
	ds_read_b128 v[122:125], v247 offset:33120
	ds_read_b128 v[126:129], v247 offset:33136
	s_nop 2
	v_cvt_pk_f16_f32 v4, v162, v163
	v_cvt_pk_f16_f32 v5, v164, v165
	v_cvt_pk_f16_f32 v6, v166, v167
	v_cvt_pk_f16_f32 v7, v168, v169
	v_cvt_pk_f16_f32 v8, v170, v171
	v_cvt_pk_f16_f32 v9, v172, v173
	v_cvt_pk_f16_f32 v10, v174, v175
	v_cvt_pk_f16_f32 v11, v176, v177
	v_cvt_pk_f16_f32 v12, v146, v147
	v_cvt_pk_f16_f32 v13, v148, v149
	v_cvt_pk_f16_f32 v14, v150, v151
	v_cvt_pk_f16_f32 v15, v152, v153
	v_cvt_pk_f16_f32 v252, v154, v155
	v_cvt_pk_f16_f32 v253, v156, v157
	v_cvt_pk_f16_f32 v254, v158, v159
	v_cvt_pk_f16_f32 v255, v160, v161
	s_waitcnt lgkmcnt(4)
	ds_read_b128 v[34:37], v246 offset:20480
	ds_read_b128 v[38:41], v246 offset:21504
	ds_read_b128 v[42:45], v246 offset:22528
	ds_read_b128 v[46:49], v246 offset:23552
	v_mfma_f32_32x32x16_f16 v[130:145], v[18:21], v[4:7], v[130:145]
	v_mfma_f32_32x32x16_f16 v[130:145], v[22:25], v[8:11], v[130:145]
	v_mfma_f32_32x32x16_f16 v[130:145], v[26:29], v[12:15], v[130:145]
	v_mfma_f32_32x32x16_f16 v[130:145], v[30:33], v[252:255], v[130:145]
	ds_read_b128 v[146:149], v247 offset:33536
	ds_read_b128 v[150:153], v247 offset:33552
	ds_read_b128 v[154:157], v247 offset:33568
	ds_read_b128 v[158:161], v247 offset:33584
	s_waitcnt lgkmcnt(4)
	ds_read_b128 v[98:101], v247 offset:33152
	ds_read_b128 v[102:105], v247 offset:33168
	ds_read_b128 v[106:109], v247 offset:33184
	ds_read_b128 v[110:113], v247 offset:33200
	ds_read_b128 v[50:53], v246 offset:24576
	ds_read_b128 v[54:57], v246 offset:25600
	ds_read_b128 v[58:61], v246 offset:26624
	ds_read_b128 v[62:65], v246 offset:27648
	v_mfma_f32_32x32x16_f16 v[114:129], v[34:37], v[4:7], v[114:129]
	v_exp_f32_e32 v130, v130
	v_exp_f32_e32 v131, v131
	v_exp_f32_e32 v132, v132
	v_exp_f32_e32 v133, v133
	v_exp_f32_e32 v134, v134
	v_exp_f32_e32 v135, v135
	v_exp_f32_e32 v136, v136
	v_exp_f32_e32 v137, v137
	v_mfma_f32_32x32x16_f16 v[114:129], v[38:41], v[8:11], v[114:129]
	v_exp_f32_e32 v138, v138
	v_exp_f32_e32 v139, v139
	v_exp_f32_e32 v140, v140
	v_exp_f32_e32 v141, v141
	v_exp_f32_e32 v142, v142
	v_exp_f32_e32 v143, v143
	v_exp_f32_e32 v144, v144
	v_exp_f32_e32 v145, v145
	v_mfma_f32_32x32x16_f16 v[114:129], v[42:45], v[12:15], v[114:129]
	v_add_f32_e32 v130, 1.0, v130
	v_add_f32_e32 v131, 1.0, v131
	v_add_f32_e32 v132, 1.0, v132
	v_add_f32_e32 v133, 1.0, v133
	v_add_f32_e32 v134, 1.0, v134
	v_add_f32_e32 v135, 1.0, v135
	v_add_f32_e32 v136, 1.0, v136
	v_add_f32_e32 v137, 1.0, v137
	v_add_f32_e32 v138, 1.0, v138
	v_add_f32_e32 v139, 1.0, v139
	v_add_f32_e32 v140, 1.0, v140
	v_add_f32_e32 v141, 1.0, v141
	v_add_f32_e32 v142, 1.0, v142
	v_add_f32_e32 v143, 1.0, v143
	v_add_f32_e32 v144, 1.0, v144
	v_add_f32_e32 v145, 1.0, v145
	v_mfma_f32_32x32x16_f16 v[114:129], v[46:49], v[252:255], v[114:129]
	v_rcp_f32_e32 v130, v130
	v_rcp_f32_e32 v131, v131
	v_rcp_f32_e32 v132, v132
	v_rcp_f32_e32 v133, v133
	v_rcp_f32_e32 v134, v134
	v_rcp_f32_e32 v135, v135
	v_rcp_f32_e32 v136, v136
	v_rcp_f32_e32 v137, v137
	v_rcp_f32_e32 v138, v138
	v_rcp_f32_e32 v139, v139
	v_rcp_f32_e32 v140, v140
	v_rcp_f32_e32 v141, v141
	v_rcp_f32_e32 v142, v142
	v_rcp_f32_e32 v143, v143
	v_rcp_f32_e32 v144, v144
	v_rcp_f32_e32 v145, v145
	s_waitcnt lgkmcnt(8)
	ds_read_b128 v[162:165], v247 offset:33600
	ds_read_b128 v[166:169], v247 offset:33616
	ds_read_b128 v[170:173], v247 offset:33632
	ds_read_b128 v[174:177], v247 offset:33648
	v_mul_f32_e32 v3, v146, v130
	v_mul_f32_e32 v16, v147, v131
	v_mul_f32_e32 v17, v148, v132
	v_fmac_f32_e32 v3, v149, v133
	v_fmac_f32_e32 v16, v150, v134
	v_fmac_f32_e32 v17, v151, v135
	v_fmac_f32_e32 v3, v152, v136
	v_fmac_f32_e32 v16, v153, v137
	v_fmac_f32_e32 v17, v154, v138
	v_fmac_f32_e32 v3, v155, v139
	v_fmac_f32_e32 v16, v156, v140
	v_fmac_f32_e32 v17, v157, v141
	v_fmac_f32_e32 v3, v158, v142
	v_fmac_f32_e32 v16, v159, v143
	v_fmac_f32_e32 v17, v160, v144
	v_fmac_f32_e32 v3, v161, v145
	s_waitcnt lgkmcnt(4)
	ds_read_b128 v[82:85], v247 offset:33216
	ds_read_b128 v[86:89], v247 offset:33232
	ds_read_b128 v[90:93], v247 offset:33248
	ds_read_b128 v[94:97], v247 offset:33264
	ds_read_b128 v[66:69], v246 offset:28672
	ds_read_b128 v[70:73], v246 offset:29696
	ds_read_b128 v[74:77], v246 offset:30720
	ds_read_b128 v[78:81], v246 offset:31744
	v_mfma_f32_32x32x16_f16 v[98:113], v[50:53], v[4:7], v[98:113]
	v_exp_f32_e32 v114, v114
	v_exp_f32_e32 v115, v115
	v_exp_f32_e32 v116, v116
	v_exp_f32_e32 v117, v117
	v_exp_f32_e32 v118, v118
	v_exp_f32_e32 v119, v119
	v_exp_f32_e32 v120, v120
	v_exp_f32_e32 v121, v121
	v_mfma_f32_32x32x16_f16 v[98:113], v[54:57], v[8:11], v[98:113]
	v_exp_f32_e32 v122, v122
	v_exp_f32_e32 v123, v123
	v_exp_f32_e32 v124, v124
	v_exp_f32_e32 v125, v125
	v_exp_f32_e32 v126, v126
	v_exp_f32_e32 v127, v127
	v_exp_f32_e32 v128, v128
	v_exp_f32_e32 v129, v129
	v_mfma_f32_32x32x16_f16 v[98:113], v[58:61], v[12:15], v[98:113]
	v_add_f32_e32 v114, 1.0, v114
	v_add_f32_e32 v115, 1.0, v115
	v_add_f32_e32 v116, 1.0, v116
	v_add_f32_e32 v117, 1.0, v117
	v_add_f32_e32 v118, 1.0, v118
	v_add_f32_e32 v119, 1.0, v119
	v_add_f32_e32 v120, 1.0, v120
	v_add_f32_e32 v121, 1.0, v121
	v_add_f32_e32 v122, 1.0, v122
	v_add_f32_e32 v123, 1.0, v123
	v_add_f32_e32 v124, 1.0, v124
	v_add_f32_e32 v125, 1.0, v125
	v_add_f32_e32 v126, 1.0, v126
	v_add_f32_e32 v127, 1.0, v127
	v_add_f32_e32 v128, 1.0, v128
	v_add_f32_e32 v129, 1.0, v129
	v_mfma_f32_32x32x16_f16 v[98:113], v[62:65], v[252:255], v[98:113]
	v_rcp_f32_e32 v114, v114
	v_rcp_f32_e32 v115, v115
	v_rcp_f32_e32 v116, v116
	v_rcp_f32_e32 v117, v117
	v_rcp_f32_e32 v118, v118
	v_rcp_f32_e32 v119, v119
	v_rcp_f32_e32 v120, v120
	v_rcp_f32_e32 v121, v121
	v_rcp_f32_e32 v122, v122
	v_rcp_f32_e32 v123, v123
	v_rcp_f32_e32 v124, v124
	v_rcp_f32_e32 v125, v125
	v_rcp_f32_e32 v126, v126
	v_rcp_f32_e32 v127, v127
	v_rcp_f32_e32 v128, v128
	v_rcp_f32_e32 v129, v129
	s_waitcnt lgkmcnt(8)
	ds_read_b128 v[18:21], v247 offset:33664
	ds_read_b128 v[22:25], v247 offset:33680
	ds_read_b128 v[26:29], v247 offset:33696
	ds_read_b128 v[30:33], v247 offset:33712
	v_fmac_f32_e32 v3, v162, v114
	v_fmac_f32_e32 v16, v163, v115
	v_fmac_f32_e32 v17, v164, v116
	v_fmac_f32_e32 v3, v165, v117
	v_fmac_f32_e32 v16, v166, v118
	v_fmac_f32_e32 v17, v167, v119
	v_fmac_f32_e32 v3, v168, v120
	v_fmac_f32_e32 v16, v169, v121
	v_fmac_f32_e32 v17, v170, v122
	v_fmac_f32_e32 v3, v171, v123
	v_fmac_f32_e32 v16, v172, v124
	v_fmac_f32_e32 v17, v173, v125
	v_fmac_f32_e32 v3, v174, v126
	v_fmac_f32_e32 v16, v175, v127
	v_fmac_f32_e32 v17, v176, v128
	v_fmac_f32_e32 v3, v177, v129
	s_waitcnt lgkmcnt(4)
	ds_read_b128 v[146:149], v247 offset:33728
	ds_read_b128 v[150:153], v247 offset:33744
	ds_read_b128 v[154:157], v247 offset:33760
	ds_read_b128 v[158:161], v247 offset:33776
	v_mfma_f32_32x32x16_f16 v[82:97], v[66:69], v[4:7], v[82:97]
	v_exp_f32_e32 v98, v98
	v_exp_f32_e32 v99, v99
	v_exp_f32_e32 v100, v100
	v_exp_f32_e32 v101, v101
	v_exp_f32_e32 v102, v102
	v_exp_f32_e32 v103, v103
	v_exp_f32_e32 v104, v104
	v_exp_f32_e32 v105, v105
	v_mfma_f32_32x32x16_f16 v[82:97], v[70:73], v[8:11], v[82:97]
	v_exp_f32_e32 v106, v106
	v_exp_f32_e32 v107, v107
	v_exp_f32_e32 v108, v108
	v_exp_f32_e32 v109, v109
	v_exp_f32_e32 v110, v110
	v_exp_f32_e32 v111, v111
	v_exp_f32_e32 v112, v112
	v_exp_f32_e32 v113, v113
	v_mfma_f32_32x32x16_f16 v[82:97], v[74:77], v[12:15], v[82:97]
	v_add_f32_e32 v98, 1.0, v98
	v_add_f32_e32 v99, 1.0, v99
	v_add_f32_e32 v100, 1.0, v100
	v_add_f32_e32 v101, 1.0, v101
	v_add_f32_e32 v102, 1.0, v102
	v_add_f32_e32 v103, 1.0, v103
	v_add_f32_e32 v104, 1.0, v104
	v_add_f32_e32 v105, 1.0, v105
	v_add_f32_e32 v106, 1.0, v106
	v_add_f32_e32 v107, 1.0, v107
	v_add_f32_e32 v108, 1.0, v108
	v_add_f32_e32 v109, 1.0, v109
	v_add_f32_e32 v110, 1.0, v110
	v_add_f32_e32 v111, 1.0, v111
	v_add_f32_e32 v112, 1.0, v112
	v_add_f32_e32 v113, 1.0, v113
	v_mfma_f32_32x32x16_f16 v[82:97], v[78:81], v[252:255], v[82:97]
	v_rcp_f32_e32 v98, v98
	v_rcp_f32_e32 v99, v99
	v_rcp_f32_e32 v100, v100
	v_rcp_f32_e32 v101, v101
	v_rcp_f32_e32 v102, v102
	v_rcp_f32_e32 v103, v103
	v_rcp_f32_e32 v104, v104
	v_rcp_f32_e32 v105, v105
	v_rcp_f32_e32 v106, v106
	v_rcp_f32_e32 v107, v107
	v_rcp_f32_e32 v108, v108
	v_rcp_f32_e32 v109, v109
	v_rcp_f32_e32 v110, v110
	v_rcp_f32_e32 v111, v111
	v_rcp_f32_e32 v112, v112
	v_rcp_f32_e32 v113, v113
	s_waitcnt lgkmcnt(4)
	v_fmac_f32_e32 v3, v18, v98
	v_fmac_f32_e32 v16, v19, v99
	v_fmac_f32_e32 v17, v20, v100
	v_fmac_f32_e32 v3, v21, v101
	v_fmac_f32_e32 v16, v22, v102
	v_fmac_f32_e32 v17, v23, v103
	v_fmac_f32_e32 v3, v24, v104
	v_fmac_f32_e32 v16, v25, v105
	v_fmac_f32_e32 v17, v26, v106
	v_fmac_f32_e32 v3, v27, v107
	v_fmac_f32_e32 v16, v28, v108
	v_fmac_f32_e32 v17, v29, v109
	v_fmac_f32_e32 v3, v30, v110
	v_fmac_f32_e32 v16, v31, v111
	v_fmac_f32_e32 v17, v32, v112
	v_fmac_f32_e32 v3, v33, v113
	v_exp_f32_e32 v82, v82
	v_exp_f32_e32 v83, v83
	v_exp_f32_e32 v84, v84
	v_exp_f32_e32 v85, v85
	v_exp_f32_e32 v86, v86
	v_exp_f32_e32 v87, v87
	v_exp_f32_e32 v88, v88
	v_exp_f32_e32 v89, v89
	v_exp_f32_e32 v90, v90
	v_exp_f32_e32 v91, v91
	v_exp_f32_e32 v92, v92
	v_exp_f32_e32 v93, v93
	v_exp_f32_e32 v94, v94
	v_exp_f32_e32 v95, v95
	v_exp_f32_e32 v96, v96
	v_exp_f32_e32 v97, v97
	v_add_f32_e32 v82, 1.0, v82
	v_add_f32_e32 v83, 1.0, v83
	v_add_f32_e32 v84, 1.0, v84
	v_add_f32_e32 v85, 1.0, v85
	v_add_f32_e32 v86, 1.0, v86
	v_add_f32_e32 v87, 1.0, v87
	v_add_f32_e32 v88, 1.0, v88
	v_add_f32_e32 v89, 1.0, v89
	v_add_f32_e32 v90, 1.0, v90
	v_add_f32_e32 v91, 1.0, v91
	v_add_f32_e32 v92, 1.0, v92
	v_add_f32_e32 v93, 1.0, v93
	v_add_f32_e32 v94, 1.0, v94
	v_add_f32_e32 v95, 1.0, v95
	v_add_f32_e32 v96, 1.0, v96
	v_add_f32_e32 v97, 1.0, v97
	v_rcp_f32_e32 v82, v82
	v_rcp_f32_e32 v83, v83
	v_rcp_f32_e32 v84, v84
	v_rcp_f32_e32 v85, v85
	v_rcp_f32_e32 v86, v86
	v_rcp_f32_e32 v87, v87
	v_rcp_f32_e32 v88, v88
	v_rcp_f32_e32 v89, v89
	v_rcp_f32_e32 v90, v90
	v_rcp_f32_e32 v91, v91
	v_rcp_f32_e32 v92, v92
	v_rcp_f32_e32 v93, v93
	v_rcp_f32_e32 v94, v94
	v_rcp_f32_e32 v95, v95
	v_rcp_f32_e32 v96, v96
	v_rcp_f32_e32 v97, v97
	s_waitcnt lgkmcnt(0)
	v_fmac_f32_e32 v3, v146, v82
	v_fmac_f32_e32 v16, v147, v83
	v_fmac_f32_e32 v17, v148, v84
	v_fmac_f32_e32 v3, v149, v85
	v_fmac_f32_e32 v16, v150, v86
	v_fmac_f32_e32 v17, v151, v87
	v_fmac_f32_e32 v3, v152, v88
	v_fmac_f32_e32 v16, v153, v89
	v_fmac_f32_e32 v17, v154, v90
	v_fmac_f32_e32 v3, v155, v91
	v_fmac_f32_e32 v16, v156, v92
	v_fmac_f32_e32 v17, v157, v93
	v_fmac_f32_e32 v3, v158, v94
	v_fmac_f32_e32 v16, v159, v95
	v_fmac_f32_e32 v17, v160, v96
	v_fmac_f32_e32 v3, v161, v97
	v_add_f32_e32 v3, v3, v16
	v_add_f32_e32 v3, v3, v17
	v_mov_b32_e32 v4, v3
	s_nop 1
	v_permlane32_swap_b32_e32 v4, v3
	s_and_saveexec_b64 s[8:9], s[10:11]
	s_cbranch_execz .LBB1_156
	s_waitcnt vmcnt(0)
	v_mul_f32_e32 v5, 0x40549a78, v238
	v_exp_f32_e32 v5, v5
	v_add_f32_e32 v3, v3, v4
	v_ashrrev_i32_e32 v7, 31, v235
	v_mov_b32_e32 v6, v235
	v_add_f32_e32 v3, v239, v3
	v_lshl_add_u64 v[6:7], v[6:7], 2, s[52:53]
	v_mul_f32_e32 v3, v5, v3
	global_store_dword v[6:7], v3, off
